# v030 plus packed fp32 multiplies / fmas unpacked into scalar pairs beside the MFMAs of the HGRN2 state update and in the attention O-rescale block
# speedup vs baseline: 1.0096x; 1.0096x over previous
; #define LAS __attribute__((address_space(3)))
; __device__ __forceinline__ float bf2f(bf16_t v) { return __uint_as_float((unsigned)v << 16); }
; __device__ __forceinline__ float sigm(float x) { return frcp(1.f + __expf(-x)); }
; __device__ __forceinline__ void hgrn_mfma(const Params& p, LAS unsigned char* lds) {
;     ...
;         bf16_t rq[8], rz[8], rv[8], rp[8];
;     ...
;         HG_LOAD(0);
;         for (int n = 0; n < T / 32; ++n) {
;             LAS unsigned char* set = lds + (n & 1) * SET_BYTES;
;             LAS unsigned char* QG = set; LAS unsigned char* KG = set + 8192; LAS unsigned char* KDT = set + 16384; LAS float* DEC = (LAS float*)(set + 24576);
;             float qv[8], fv[8], vv[8], vp[8];
; #pragma unroll
;             for (int i = 0; i < 8; ++i) { qv[i] = bf2f(rq[i]); vv[i] = bf2f(rv[i]); fv[i] = bf2f(rz[i]); vp[i] = bf2f(rp[i]); }
;             if (n + 1 < T / 32) HG_LOAD(n + 1);
;             float Pl[8]; float P = 1.f;
; #pragma unroll
;             for (int i = 0; i < 8; ++i) { fv[i] = lb + (1.f - lb) * sigm(fv[i]); P *= fv[i]; Pl[i] = P; }
.LBB0_275:
	v_add_u32_e32 v188, s55, v40
	v_add_u32_e32 v189, s54, v133
	s_bitcmp1_b32 s56, 0
	s_waitcnt vmcnt(31)
	v_lshlrev_b32_e32 v0, 16, v135
	s_waitcnt vmcnt(25)
	v_lshlrev_b32_e32 v53, 16, v138
	s_waitcnt vmcnt(1)
	v_lshlrev_b32_e32 v199, 16, v158
	v_add_u32_e32 v158, s54, v132
	v_add_u32_e32 v184, s55, v41
	v_add_u32_e32 v135, 32, v188
	v_add_u32_e32 v138, 0x7df, v189
	s_cselect_b32 s46, 0x6200, 0
	v_add_u32_e32 v2, 0x7df, v158
	v_add_u32_e32 v3, 32, v184
	v_cndmask_b32_e64 v135, v138, v135, s[18:19]
	s_add_i32 s57, s46, 0
	v_lshlrev_b32_e32 v193, 16, v139
	v_cndmask_b32_e64 v2, v2, v3, s[18:19]
	v_mad_i64_i32 v[138:139], s[46:47], v135, s52, v[44:45]
	v_add_u32_e32 v135, 0x7de, v158
	v_add_u32_e32 v140, 33, v184
	v_mul_lo_u32 v2, v2, s51
	v_cndmask_b32_e64 v135, v135, v140, s[18:19]
	v_ashrrev_i32_e32 v3, 31, v2
	v_mul_lo_u32 v140, v135, s51
	v_lshlrev_b32_e32 v55, 16, v141
	v_lshl_add_u64 v[2:3], v[2:3], 1, v[44:45]
	v_ashrrev_i32_e32 v141, 31, v140
	v_add_u32_e32 v135, 33, v188
	v_add_u32_e32 v142, 0x7de, v189
	v_lshlrev_b32_e32 v51, 16, v137
	v_lshlrev_b32_e32 v192, 16, v136
	v_lshl_add_u64 v[136:137], v[2:3], 0, s[42:43]
	v_lshl_add_u64 v[140:141], v[140:141], 1, v[44:45]
	v_cndmask_b32_e64 v135, v142, v135, s[18:19]
	v_lshlrev_b32_e32 v194, 16, v144
	v_lshlrev_b32_e32 v195, 16, v145
	v_lshl_add_u64 v[144:145], v[140:141], 0, s[42:43]
	v_mad_i64_i32 v[146:147], s[46:47], v135, s52, v[44:45]
	global_load_ushort v135, v[2:3], off
	global_load_ushort v167, v[2:3], off offset:2048
	s_nop 0
	global_load_ushort v137, v[136:137], off
	s_nop 0
	global_load_ushort v143, v[138:139], off offset:2048
	global_load_ushort v136, v[140:141], off
	global_load_ushort v168, v[140:141], off offset:2048
	s_nop 0
	global_load_ushort v138, v[144:145], off
	global_load_ushort v140, v[146:147], off offset:2048
	v_add_u32_e32 v139, 34, v188
	v_add_u32_e32 v141, 0x7dd, v189
	v_add_u32_e32 v2, 0x7dd, v158
	v_add_u32_e32 v3, 34, v184
	v_cndmask_b32_e64 v139, v141, v139, s[18:19]
	v_cndmask_b32_e64 v2, v2, v3, s[18:19]
	v_mad_i64_i32 v[146:147], s[46:47], v139, s52, v[44:45]
	v_add_u32_e32 v139, 0x7dc, v158
	v_add_u32_e32 v141, 35, v184
	v_mul_lo_u32 v2, v2, s51
	v_cndmask_b32_e64 v139, v139, v141, s[18:19]
	v_ashrrev_i32_e32 v3, 31, v2
	v_mul_lo_u32 v148, v139, s51
	v_lshlrev_b32_e32 v204, 16, v149
	v_lshl_add_u64 v[2:3], v[2:3], 1, v[44:45]
	v_ashrrev_i32_e32 v149, 31, v148
	v_add_u32_e32 v139, 35, v188
	v_add_u32_e32 v141, 0x7dc, v189
	v_lshl_add_u64 v[144:145], v[2:3], 0, s[42:43]
	v_lshl_add_u64 v[148:149], v[148:149], 1, v[44:45]
	v_cndmask_b32_e64 v139, v141, v139, s[18:19]
	v_lshlrev_b32_e32 v196, 16, v151
	v_lshlrev_b32_e32 v205, 16, v153
	v_lshl_add_u64 v[150:151], v[148:149], 0, s[42:43]
	v_mad_i64_i32 v[152:153], s[46:47], v139, s52, v[44:45]
	global_load_ushort v139, v[2:3], off
	global_load_ushort v169, v[2:3], off offset:2048
	global_load_ushort v141, v[144:145], off
	s_nop 0
	global_load_ushort v146, v[146:147], off offset:2048
	s_nop 0
	global_load_ushort v144, v[148:149], off
	global_load_ushort v170, v[148:149], off offset:2048
	global_load_ushort v145, v[150:151], off
	global_load_ushort v142, v[152:153], off offset:2048
	v_add_u32_e32 v147, 48, v188
	v_add_u32_e32 v148, 0x7cf, v189
	v_cndmask_b32_e64 v147, v148, v147, s[18:19]
	v_add_u32_e32 v2, 0x7db, v158
	v_add_u32_e32 v3, 36, v184
	v_mad_i64_i32 v[152:153], s[46:47], v147, s52, v[44:45]
	v_add_u32_e32 v147, 0x7da, v158
	v_add_u32_e32 v148, 37, v184
	v_cndmask_b32_e64 v2, v2, v3, s[18:19]
	v_cndmask_b32_e64 v147, v147, v148, s[18:19]
	v_mul_lo_u32 v2, v2, s51
	v_mul_lo_u32 v148, v147, s51
	v_mul_f32_e32 v51, 0xbfb8aa3b, v51
	v_ashrrev_i32_e32 v3, 31, v2
	v_ashrrev_i32_e32 v149, 31, v148
	v_exp_f32_e32 v51, v51
	v_mul_f32_e32 v53, 0xbfb8aa3b, v53
	v_lshlrev_b32_e32 v197, 16, v154
	v_lshlrev_b32_e32 v206, 16, v155
	v_lshl_add_u64 v[2:3], v[2:3], 1, v[44:45]
	v_lshl_add_u64 v[154:155], v[148:149], 1, v[44:45]
	v_add_u32_e32 v147, 49, v188
	v_add_u32_e32 v148, 0x7ce, v189
	v_exp_f32_e32 v53, v53
	v_lshl_add_u64 v[150:151], v[2:3], 0, s[42:43]
	v_cndmask_b32_e64 v147, v148, v147, s[18:19]
	v_lshlrev_b32_e32 v198, 16, v156
	v_lshlrev_b32_e32 v207, 16, v157
	v_lshl_add_u64 v[156:157], v[154:155], 0, s[42:43]
	v_mad_i64_i32 v[178:179], s[46:47], v147, s52, v[44:45]
	global_load_ushort v149, v[2:3], off
	global_load_ushort v173, v[2:3], off offset:2048
	s_nop 0
	global_load_ushort v151, v[150:151], off
	s_nop 0
	global_load_ushort v147, v[152:153], off offset:2048
	s_nop 0
	global_load_ushort v153, v[154:155], off
	global_load_ushort v174, v[154:155], off offset:2048
	s_nop 0
	global_load_ushort v154, v[156:157], off
	global_load_ushort v148, v[178:179], off offset:2048
	v_add_u32_e32 v150, 50, v188
	v_add_u32_e32 v152, 0x7cd, v189
	v_add_u32_e32 v2, 0x7d9, v158
	v_add_u32_e32 v3, 38, v184
	v_cndmask_b32_e64 v150, v152, v150, s[18:19]
	v_add_f32_e32 v51, 1.0, v51
	v_cndmask_b32_e64 v2, v2, v3, s[18:19]
	v_mad_i64_i32 v[182:183], s[46:47], v150, s52, v[44:45]
	v_add_u32_e32 v150, 0x7d8, v158
	v_add_u32_e32 v152, 39, v184
	v_rcp_f32_e32 v191, v51
	v_add_f32_e32 v51, 1.0, v53
	v_mul_lo_u32 v2, v2, s51
	v_cndmask_b32_e64 v150, v150, v152, s[18:19]
	v_rcp_f32_e32 v190, v51
	v_mul_f32_e32 v51, 0xbfb8aa3b, v196
	v_ashrrev_i32_e32 v3, 31, v2
	v_mul_lo_u32 v178, v150, s51
	v_add_u32_e32 v150, 51, v188
	v_add_u32_e32 v152, 0x7cc, v189
	v_exp_f32_e32 v51, v51
	v_lshl_add_u64 v[2:3], v[2:3], 1, v[44:45]
	v_ashrrev_i32_e32 v179, 31, v178
	v_cndmask_b32_e64 v150, v152, v150, s[18:19]
	v_lshl_add_u64 v[156:157], v[2:3], 0, s[42:43]
	v_lshl_add_u64 v[184:185], v[178:179], 1, v[44:45]
; #define LAS __attribute__((address_space(3)))
; __device__ __forceinline__ bf16_t f2bf(float a) { return (bf16_t)(pk2(a, 0.f) & 0xffffu); }
; __device__ __forceinline__ float frcp(float x) { return __builtin_amdgcn_rcpf(x); }
; __device__ __forceinline__ float sigm(float x) { return frcp(1.f + __expf(-x)); }
; __device__ __forceinline__ float silu(float x) { return x * frcp(1.f + __expf(-x)); }
; __device__ __forceinline__ void hgrn_mfma(const Params& p, LAS unsigned char* lds) {
;     ...
;             float Pl[8]; float P = 1.f;
; #pragma unroll
;             for (int i = 0; i < 8; ++i) { fv[i] = lb + (1.f - lb) * sigm(fv[i]); P *= fv[i]; Pl[i] = P; }
;             const float p0 = __shfl(P, fr), p1 = __shfl(P, fr + 16), p2 = __shfl(P, fr + 32), p3 = __shfl(P, fr + 48);
;             const float pre = (fq > 0 ? p0 : 1.f) * (fq > 1 ? p1 : 1.f) * (fq > 2 ? p2 : 1.f), tot = (p0 * p1) * (p2 * p3);
;             float kd[8];
; #pragma unroll
;             for (int i = 0; i < 8; ++i) {
;                 const int c = 8 * fq + i; const float E = pre * Pl[i], rE = frcp(E), k = 1.f - fv[i];
;                 *(LAS bf16_t*)(QG + rm_byte(c, d)) = f2bf(silu(qv[i]) * E);
;                 *(LAS bf16_t*)(KG + rm_byte(c, d)) = f2bf(k * rE);
;                 kd[i] = k * tot * rE;
;             }
	v_mad_i64_i32 v[188:189], s[46:47], v150, s52, v[44:45]
	v_lshl_add_u64 v[186:187], v[184:185], 0, s[42:43]
	global_load_ushort v155, v[2:3], off
	global_load_ushort v178, v[2:3], off offset:2048
	s_nop 0
	global_load_ushort v156, v[156:157], off
	s_nop 0
	global_load_ushort v150, v[182:183], off offset:2048
	global_load_ushort v157, v[184:185], off
	global_load_ushort v179, v[184:185], off offset:2048
	global_load_ushort v158, v[186:187], off
	global_load_ushort v152, v[188:189], off offset:2048
	v_mul_f32_e32 v188, 0xbfb8aa3b, v192
	v_add_f32_e32 v51, 1.0, v51
	v_exp_f32_e32 v188, v188
	v_rcp_f32_e32 v186, v51
	v_mul_f32_e32 v51, 0xbfb8aa3b, v199
	v_exp_f32_e32 v51, v51
	v_add_f32_e32 v188, 1.0, v188
	v_rcp_f32_e32 v189, v188
	v_mul_f32_e32 v2, 0xbfb8aa3b, v55
	v_add_f32_e32 v51, 1.0, v51
	v_mul_f32_e32 v3, 0xbfb8aa3b, v195
	v_rcp_f32_e32 v188, v51
	v_mul_f32_e32 v51, 0xbfb8aa3b, v193
	v_exp_f32_e32 v2, v2
	v_exp_f32_e32 v3, v3
	v_exp_f32_e32 v51, v51
	v_mul_f32_e32 v208, v189, v192
	v_mul_f32_e32 v189, 0xbfb8aa3b, v194
	v_exp_f32_e32 v189, v189
	v_add_f32_e32 v2, 1.0, v2
	v_add_f32_e32 v3, 1.0, v3
	v_add_f32_e32 v51, 1.0, v51
	v_rcp_f32_e32 v2, v2
	v_rcp_f32_e32 v3, v3
	v_mul_f32_e32 v53, 0xbfb8aa3b, v197
	v_rcp_f32_e32 v51, v51
	v_exp_f32_e32 v53, v53
	v_mul_f32_e32 v55, 0xbfb8aa3b, v198
	v_add_f32_e32 v189, 1.0, v189
	v_exp_f32_e32 v55, v55
	v_rcp_f32_e32 v189, v189
	v_fma_f32 v182, v48, v190, v46
	v_fma_f32 v183, v49, v191, v47
	v_mul_f32_e32 v210, v51, v193
	v_pk_mul_f32 v[184:185], v[182:183], v[182:183] op_sel:[0,1] op_sel_hi:[1,0]
	v_fma_f32 v192, v48, v2, v46
	v_fma_f32 v193, v49, v3, v47
	v_add_f32_e32 v53, 1.0, v53
	v_mov_b32_e32 v187, v184
	v_mov_b32_e32 v2, v52
	v_mov_b32_e32 v3, v192
	v_rcp_f32_e32 v53, v53
	v_add_f32_e32 v55, 1.0, v55
	v_mul_f32_e32 v212, v189, v194
	v_mul_f32_e32 v194, v2, v186
	v_mul_f32_e32 v195, v3, v187
	v_mov_b32_e32 v51, v193
	v_rcp_f32_e32 v55, v55
	v_fma_f32 v186, v2, v186, v50
	v_fma_f32 v187, v3, v187, v51
	v_mul_f32_e32 v196, v50, v194
	v_mul_f32_e32 v197, v51, v195
	v_fma_f32 v53, v52, v53, v50
	v_mov_b32_e32 v187, v197
	v_pk_mul_f32 v[198:199], v[186:187], v[196:197] op_sel:[0,1] op_sel_hi:[1,0]
	v_fma_f32 v55, v52, v55, v50
	v_mov_b32_e32 v189, v198
	v_mul_f32_e32 v200, v52, v188
	v_mul_f32_e32 v201, v53, v189
	v_mul_f32_e32 v185, 0xbfb8aa3b, v0
	v_fma_f32 v188, v52, v188, v54
	v_fma_f32 v189, v53, v189, v55
	v_mul_f32_e32 v51, v55, v201
	v_exp_f32_e32 v185, v185
	v_mul_f32_e32 v189, v188, v51
	ds_bpermute_b32 v2, v56, v189
	ds_bpermute_b32 v202, v57, v189
	ds_bpermute_b32 v3, v58, v189
	v_add_f32_e32 v185, 1.0, v185
	v_rcp_f32_e32 v185, v185
	v_pk_add_f32 v[190:191], v[182:183], 1.0 op_sel_hi:[1,0] neg_lo:[1,0] neg_hi:[1,0]
	s_waitcnt lgkmcnt(2)
	v_cndmask_b32_e64 v182, v2, 1.0, s[4:5]
	s_waitcnt lgkmcnt(1)
	v_cndmask_b32_e64 v194, 1.0, v202, s[6:7]
	v_mul_f32_e32 v182, v182, v194
	s_waitcnt lgkmcnt(0)
	v_cndmask_b32_e64 v194, 1.0, v3, s[8:9]
	v_mul_f32_e32 v194, v182, v194
	v_mul_f32_e32 v0, v185, v0
	v_mul_f32_e32 v182, v183, v194
	v_mul_f32_e32 v0, v0, v182
	v_add_u32_e32 v185, s57, v97
	ds_bpermute_b32 v203, v59, v189
	v_rcp_f32_e32 v183, v182
	v_cvt_pk_bf16_f32 v0, v0, s0
	ds_write_b16 v185, v0
	v_mul_f32_e32 v0, v184, v194
	v_rcp_f32_e32 v182, v0
	v_mul_f32_e32 v0, v208, v0
	v_mul_f32_e32 v184, v191, v183
	v_add_u32_e32 v209, s57, v125
	s_waitcnt lgkmcnt(1)
	v_mul_f32_e32 v2, v2, v202
	v_mul_f32_e32 v3, v3, v203
	v_cvt_pk_bf16_f32 v0, v0, s0
	v_cvt_pk_bf16_f32 v184, v184, s0
	v_pk_mul_f32 v[2:3], v[2:3], v[2:3] op_sel:[0,1] op_sel_hi:[1,0]
	ds_write_b16 v185, v184 offset:8192
	ds_write_b16 v209, v0 offset:256
	v_mul_f32_e32 v0, v190, v182
	v_pk_mul_f32 v[184:185], v[190:191], v[2:3] op_sel_hi:[1,0]
	v_cvt_pk_bf16_f32 v0, v0, s0
	v_mul_f32_e32 v184, v182, v184
	v_mul_f32_e32 v185, v183, v185
	ds_write_b16 v209, v0 offset:8448
	v_mul_f32_e32 v0, v195, v194
	v_mul_f32_e32 v195, v197, v194
	v_pk_mov_b32 v[182:183], v[184:185], v[184:185] op_sel:[1,0]
	v_rcp_f32_e32 v184, v0
	v_rcp_f32_e32 v185, v195
	v_mul_f32_e32 v0, v210, v0
	v_pk_add_f32 v[190:191], v[192:193], 1.0 op_sel_hi:[1,0] neg_lo:[1,0] neg_hi:[1,0]
	v_add_u32_e32 v211, s57, v126
	v_cvt_pk_bf16_f32 v0, v0, s0
	v_pk_mul_f32 v[192:193], v[190:191], v[2:3] op_sel_hi:[1,0]
	ds_write_b16 v211, v0 offset:512
	v_mul_f32_e32 v0, v190, v184
	v_mul_f32_e32 v192, v184, v192
	v_mul_f32_e32 v193, v185, v193
	v_mul_f32_e32 v184, 0xbfb8aa3b, v204
	v_cvt_pk_bf16_f32 v0, v0, s0
	v_exp_f32_e32 v184, v184
	ds_write_b16 v211, v0 offset:8704
	v_mul_f32_e32 v0, v212, v195
	v_add_u32_e32 v187, s57, v127
	v_cvt_pk_bf16_f32 v0, v0, s0
	ds_write_b16 v187, v0 offset:768
	v_mul_f32_e32 v0, v191, v185
	v_cvt_pk_bf16_f32 v0, v0, s0
	v_add_f32_e32 v184, 1.0, v184
	v_rcp_f32_e32 v185, v184
	ds_write_b16 v187, v0 offset:8960
	v_mul_f32_e32 v187, 0xbfb8aa3b, v205
	v_exp_f32_e32 v187, v187
	v_mul_f32_e32 v0, v198, v194
	v_mul_f32_e32 v185, v185, v204
	v_rcp_f32_e32 v184, v0
	v_mul_f32_e32 v0, v185, v0
	v_add_f32_e32 v185, 1.0, v187
	v_rcp_f32_e32 v187, v185
	v_cvt_pk_bf16_f32 v0, v0, s0
	v_add_u32_e32 v190, s57, v128
	ds_write_b16 v190, v0 offset:1024
	v_mul_f32_e32 v0, v201, v194
	v_mul_f32_e32 v187, v187, v205
	v_rcp_f32_e32 v185, v0
	v_mul_f32_e32 v0, v187, v0
	v_mov_b32_e32 v187, v53
	v_pk_add_f32 v[186:187], v[186:187], 1.0 op_sel_hi:[1,0] neg_lo:[1,0] neg_hi:[1,0]
	v_cvt_pk_bf16_f32 v0, v0, s0
	v_mul_f32_e32 v53, v186, v184
	v_cvt_pk_bf16_f32 v53, v53, s0
	ds_write_b16 v190, v53 offset:9216
	v_mul_f32_e32 v53, 0xbfb8aa3b, v206
	v_exp_f32_e32 v53, v53
	v_add_u32_e32 v195, s57, v129
	ds_write_b16 v195, v0 offset:1280
	v_mul_f32_e32 v0, v187, v185
; __device__ __forceinline__ void hgrn_mfma(const Params& p, LAS unsigned char* lds) {
;     ...
;             float kd[8];
; #pragma unroll
;             for (int i = 0; i < 8; ++i) {
;                 const int c = 8 * fq + i; const float E = pre * Pl[i], rE = frcp(E), k = 1.f - fv[i];
;                 *(LAS bf16_t*)(QG + rm_byte(c, d)) = f2bf(silu(qv[i]) * E);
;                 *(LAS bf16_t*)(KG + rm_byte(c, d)) = f2bf(k * rE);
;                 kd[i] = k * tot * rE;
;             }
;             { u32x4 wv; wv.x = pk2(kd[0], kd[1]); wv.y = pk2(kd[2], kd[3]); wv.z = pk2(kd[4], kd[5]); wv.w = pk2(kd[6], kd[7]);
;               *(LAS u32x4*)(KDT + d * 64 + ((fq ^ ((d >> 2) & 3)) << 4)) = wv; }
;             if (fq == 0) DEC[d] = tot;
;             const bf16x8 vB = pack8((f32x4){vv[0], vv[1], vv[2], vv[3]}, (f32x4){vv[4], vv[5], vv[6], vv[7]});
;             const bf16x8 vP = pack8((f32x4){vp[0], vp[1], vp[2], vp[3]}, (f32x4){vp[4], vp[5], vp[6], vp[7]});
;             __syncthreads();
;             f32x4 at00 = {0.f, 0.f, 0.f, 0.f}, at01 = at00, at11 = at00;
; #pragma unroll
;             for (int ks = 0; ks < 4; ++ks) {
;                 const int d0 = 32 * ks + 8 * fq;
;                 const bf16x8 kg0 = *(const LAS bf16x8*)(KG + rm_byte(fr, d0)), kg1 = *(const LAS bf16x8*)(KG + rm_byte(16 + fr, d0));
;                 const bf16x8 qg0 = *(const LAS bf16x8*)(QG + rm_byte(fr, d0)), qg1 = *(const LAS bf16x8*)(QG + rm_byte(16 + fr, d0));
;                 at00 = __builtin_amdgcn_mfma_f32_16x16x32_bf16(kg0, qg0, at00, 0, 0, 0);
;                 at01 = __builtin_amdgcn_mfma_f32_16x16x32_bf16(kg0, qg1, at01, 0, 0, 0);
;                 at11 = __builtin_amdgcn_mfma_f32_16x16x32_bf16(kg1, qg1, at11, 0, 0, 0);
;             }
; #pragma unroll
;             for (int j = 0; j < 4; ++j) { const bool ok = (4 * fq + j) <= fr; at00[j] = ok ? at00[j] : 0.f; at11[j] = ok ? at11[j] : 0.f; }
;             const bf16x8 bi0 = pack8(at00, (f32x4){0.f, 0.f, 0.f, 0.f}), bi1 = pack8(at01, at11);
;             f32x4 o0 = {0.f, 0.f, 0.f, 0.f}, o1 = o0;
;             o0 = __builtin_amdgcn_mfma_f32_16x16x32_bf16(vP, bi0, o0, 0, 0, 0);
;             o1 = __builtin_amdgcn_mfma_f32_16x16x32_bf16(vP, bi1, o1, 0, 0, 0);
; #pragma unroll
;             for (int ks = 0; ks < 4; ++ks) {
;                 const bf16x8 sb = pack8(S[2 * ks], S[2 * ks + 1]);
	v_add_f32_e32 v53, 1.0, v53
	v_rcp_f32_e32 v53, v53
	v_cvt_pk_bf16_f32 v0, v0, s0
	ds_write_b16 v195, v0 offset:9472
	v_mul_f32_e32 v0, v51, v194
	v_mul_f32_e32 v51, v53, v206
	v_mul_f32_e32 v53, 0xbfb8aa3b, v207
	v_exp_f32_e32 v53, v53
	v_pk_mul_f32 v[190:191], v[186:187], v[2:3] op_sel_hi:[1,0]
	v_mov_b32_e32 v186, v55
	v_mul_f32_e32 v190, v184, v190
	v_mul_f32_e32 v191, v185, v191
	v_add_f32_e32 v53, 1.0, v53
	v_rcp_f32_e32 v184, v0
	v_mul_f32_e32 v0, v51, v0
	v_rcp_f32_e32 v53, v53
	v_cvt_pk_bf16_f32 v0, v0, s0
	v_add_u32_e32 v51, s57, v130
	ds_write_b16 v51, v0 offset:1536
	v_mul_f32_e32 v0, v189, v194
	v_rcp_f32_e32 v185, v0
	v_mov_b32_e32 v187, v188
	v_mul_f32_e32 v53, v53, v207
	v_pk_add_f32 v[186:187], v[186:187], 1.0 op_sel_hi:[1,0] neg_lo:[1,0] neg_hi:[1,0]
	v_mul_f32_e32 v0, v53, v0
	v_mul_f32_e32 v55, v186, v184
	v_cvt_pk_bf16_f32 v0, v0, s0
	v_add_u32_e32 v53, s57, v131
	v_cvt_pk_bf16_f32 v55, v55, s0
	ds_write_b16 v51, v55 offset:9728
	v_pk_mul_f32 v[188:189], v[186:187], v[2:3] op_sel_hi:[1,0]
	ds_write_b16 v53, v0 offset:1792
	v_mul_f32_e32 v0, v187, v185
	v_mul_f32_e32 v188, v184, v188
	v_mul_f32_e32 v189, v185, v189
	v_cvt_pk_bf16_f32 v0, v0, s0
	v_add_u32_e32 v3, s57, v60
	ds_write_b16 v53, v0 offset:9984
	v_cvt_pk_bf16_f32 v182, v182, v183
	v_cvt_pk_bf16_f32 v183, v192, v193
	v_cvt_pk_bf16_f32 v184, v190, v191
	v_cvt_pk_bf16_f32 v185, v188, v189
	v_add_u32_e32 v0, v3, v61
	ds_write_b128 v0, v[182:185] offset:16384
	s_and_saveexec_b64 s[46:47], s[4:5]
	v_add_u32_e32 v0, v3, v118
	ds_write_b32 v0, v2 offset:24576
	s_or_b64 exec, exec, s[46:47]
	v_add_u32_e32 v2, s57, v98
	s_waitcnt lgkmcnt(0)
	s_barrier
	ds_read_b128 v[182:185], v2 offset:8192
	v_lshlrev_b32_e32 v3, 16, v5
	v_add_u32_e32 v5, s57, v99
	ds_read_b128 v[186:189], v5 offset:8192
	ds_read_b128 v[190:193], v2
	ds_read_b128 v[194:197], v5
	v_add_u32_e32 v5, s57, v100
	ds_read_b128 v[198:201], v5 offset:8192
	v_add_u32_e32 v51, s57, v101
	ds_read_b128 v[202:205], v51 offset:8192
	ds_read_b128 v[206:209], v5
	v_add_u32_e32 v5, s57, v102
	s_waitcnt lgkmcnt(4)
	v_mfma_f32_16x16x32_bf16 v[190:193], v[182:185], v[190:193], 0
	ds_read_b128 v[210:213], v51
	ds_read_b128 v[214:217], v5 offset:8192
	v_add_u32_e32 v51, s57, v103
	s_waitcnt lgkmcnt(5)
	v_mfma_f32_16x16x32_bf16 v[186:189], v[186:189], v[194:197], 0
	v_lshlrev_b32_e32 v0, 16, v171
	v_lshlrev_b32_e32 v55, 16, v180
	s_waitcnt vmcnt(32)
	v_lshlrev_b32_e32 v171, 16, v181
	s_waitcnt lgkmcnt(2)
	v_mfma_f32_16x16x32_bf16 v[190:193], v[198:201], v[206:209], v[190:193]
	ds_read_b128 v[206:209], v51 offset:8192
	ds_read_b128 v[218:221], v5
	v_add_u32_e32 v5, s57, v104
	ds_read_b128 v[224:227], v5 offset:8192
	s_waitcnt lgkmcnt(4)
	v_mfma_f32_16x16x32_bf16 v[186:189], v[202:205], v[210:213], v[186:189]
	ds_read_b128 v[202:205], v51
	v_add_u32_e32 v51, s57, v105
	v_lshlrev_b32_e32 v2, 16, v175
	v_mfma_f32_16x16x32_bf16 v[180:183], v[182:185], v[194:197], 0
	v_lshlrev_b32_e32 v53, 16, v177
	s_add_i32 s56, s56, 1
	s_waitcnt lgkmcnt(2)
	v_mfma_f32_16x16x32_bf16 v[190:193], v[214:217], v[218:221], v[190:193]
	ds_read_b128 v[218:221], v51 offset:8192
	ds_read_b128 v[228:231], v5
	v_lshlrev_b32_e32 v5, 16, v172
	s_waitcnt lgkmcnt(2)
	v_mfma_f32_16x16x32_bf16 v[186:189], v[206:209], v[202:205], v[186:189]
	ds_read_b128 v[206:209], v51
	v_lshlrev_b32_e32 v51, 16, v176
	v_mfma_f32_16x16x32_bf16 v[180:183], v[198:201], v[210:213], v[180:183]
	s_waitcnt lgkmcnt(1)
	v_mfma_f32_16x16x32_bf16 v[190:193], v[224:227], v[228:231], v[190:193]
	v_mfma_f32_16x16x32_bf16 v[180:183], v[214:217], v[202:205], v[180:183]
	s_waitcnt lgkmcnt(0)
	v_mfma_f32_16x16x32_bf16 v[186:189], v[218:221], v[206:209], v[186:189]
	v_cvt_pk_bf16_f32 v218, v0, v3
	v_cvt_pk_bf16_f32 v219, v2, v5
	v_cvt_pk_bf16_f32 v220, v53, v51
	v_cvt_pk_bf16_f32 v221, v55, v171
	s_nop 0
	v_cndmask_b32_e64 v0, v190, 0, s[10:11]
	v_cndmask_b32_e64 v2, 0, v191, s[12:13]
	v_cndmask_b32_e64 v3, v192, 0, s[14:15]
	v_cndmask_b32_e64 v5, v193, 0, s[16:17]
	v_mfma_f32_16x16x32_bf16 v[180:183], v[224:227], v[206:209], v[180:183]
	v_cvt_pk_bf16_f32 v2, v0, v2
	v_cvt_pk_bf16_f32 v3, v3, v5
	v_mov_b32_e32 v5, v4
	v_add_u32_e32 v0, s57, v62
	v_cndmask_b32_e64 v51, v186, 0, s[10:11]
	v_cndmask_b32_e64 v53, 0, v187, s[12:13]
	v_mfma_f32_16x16x32_bf16 v[184:187], v[218:221], v[2:5], 0
	v_add_u32_e32 v2, s57, v63
	v_add_u32_e32 v3, v0, v106
	v_cndmask_b32_e64 v55, v188, 0, s[14:15]
	v_cndmask_b32_e64 v171, v189, 0, s[16:17]
	v_add_u32_e32 v5, v0, v107
	ds_read_b64 v[192:193], v3
	ds_read_b64 v[194:195], v5
	v_add_u32_e32 v3, v2, v106
	v_cvt_pk_bf16_f32 v180, v180, v181
	v_cvt_pk_bf16_f32 v181, v182, v183
	v_cvt_pk_bf16_f32 v182, v51, v53
	v_cvt_pk_bf16_f32 v183, v55, v171
	v_cvt_pk_bf16_f32 v188, v34, v35
	v_cvt_pk_bf16_f32 v189, v36, v37
	v_cvt_pk_bf16_f32 v190, v30, v31
	v_cvt_pk_bf16_f32 v191, v32, v33
	v_add_u32_e32 v5, v2, v107
	ds_read_b64 v[196:197], v3
	ds_read_b64 v[198:199], v5
	v_mfma_f32_16x16x32_bf16 v[180:183], v[218:221], v[180:183], 0
	v_add_u32_e32 v53, v0, v108
	v_add_u32_e32 v55, v0, v109
	v_lshlrev_b32_e32 v5, 16, v160
	s_waitcnt lgkmcnt(2)
	v_mfma_f32_16x16x32_bf16 v[184:187], v[188:191], v[192:195], v[184:187]
	ds_read_b64 v[192:193], v53
	ds_read_b64 v[194:195], v55
	v_add_u32_e32 v53, v2, v108
	v_add_u32_e32 v55, v2, v109
	s_waitcnt lgkmcnt(2)
	v_mfma_f32_16x16x32_bf16 v[180:183], v[188:191], v[196:199], v[180:183]
	v_cvt_pk_bf16_f32 v188, v26, v27
	v_cvt_pk_bf16_f32 v189, v28, v29
	v_cvt_pk_bf16_f32 v190, v22, v23
	v_cvt_pk_bf16_f32 v191, v24, v25
	ds_read_b64 v[196:197], v53
	ds_read_b64 v[198:199], v55
	v_add_u32_e32 v160, v0, v110
	s_waitcnt lgkmcnt(2)
; #define LAS __attribute__((address_space(3)))
; __device__ __forceinline__ unsigned pk2(float a, float b) { f32x2 v = {a, b}; bf16x2_t r = __builtin_convertvector(v, bf16x2_t); return __builtin_bit_cast(unsigned, r); }
; __device__ __forceinline__ bf16x8 pack8(const f32x4& a, const f32x4& b) { u32x4 w; w.x = pk2(a.x, a.y); w.y = pk2(a.z, a.w); w.z = pk2(b.x, b.y); w.w = pk2(b.z, b.w); return __builtin_bit_cast(bf16x8, w); }
; __device__ __forceinline__ void hgrn_mfma(const Params& p, LAS unsigned char* lds) {
;     ...
;             for (int ks = 0; ks < 4; ++ks) {
;                 const bf16x8 sb = pack8(S[2 * ks], S[2 * ks + 1]);
;                 const int da = 32 * ks + 4 * fq, db = da + 16;
;                 const bf16x4 q0a = *(const LAS bf16x4*)(QG + rm_byte(fr, da)), q0b = *(const LAS bf16x4*)(QG + rm_byte(fr, db));
;                 const bf16x4 q1a = *(const LAS bf16x4*)(QG + rm_byte(16 + fr, da)), q1b = *(const LAS bf16x4*)(QG + rm_byte(16 + fr, db));
;                 const bf16x8 qp0 = {q0a[0], q0a[1], q0a[2], q0a[3], q0b[0], q0b[1], q0b[2], q0b[3]}, qp1 = {q1a[0], q1a[1], q1a[2], q1a[3], q1b[0], q1b[1], q1b[2], q1b[3]};
;                 o0 = __builtin_amdgcn_mfma_f32_16x16x32_bf16(sb, qp0, o0, 0, 0, 0);
;                 o1 = __builtin_amdgcn_mfma_f32_16x16x32_bf16(sb, qp1, o1, 0, 0, 0);
;             }
;             { const int c0 = fr, c1 = 16 + fr; const int t0 = dir ? (T - 1 - (32 * n + c0)) : (32 * n + c0), t1 = dir ? (T - 1 - (32 * n + c1)) : (32 * n + c1);
;               bf16_t* ob = oscr + ((size_t)dir * M + (size_t)b * T) * 1024 + h * 128 + 16 * w + 4 * fq;
;               u32x2 w0; w0.x = pk2(o0[0], o0[1]); w0.y = pk2(o0[2], o0[3]); u32x2 w1; w1.x = pk2(o1[0], o1[1]); w1.y = pk2(o1[2], o1[3]);
;               *(u32x2*)(ob + (size_t)t0 * 1024) = w0; *(u32x2*)(ob + (size_t)t1 * 1024) = w1; }
; #pragma unroll
;             for (int mi = 0; mi < 8; ++mi) {
;                 const int dr = 16 * mi + fr;
;                 const bf16x8 ka = *(const LAS bf16x8*)(KDT + dr * 64 + ((fq ^ ((dr >> 2) & 3)) << 4));
;                 const f32x4 dc = *(const LAS f32x4*)(DEC + 16 * mi + 4 * fq);
;                 S[mi] = __builtin_amdgcn_mfma_f32_16x16x32_bf16(ka, vB, S[mi] * dc, 0, 0, 0);
;             }
	v_mfma_f32_16x16x32_bf16 v[184:187], v[188:191], v[192:195], v[184:187]
	v_lshlrev_b32_e32 v53, 16, v161
	v_add_u32_e32 v161, v0, v111
	ds_read_b64 v[192:193], v160
	ds_read_b64 v[194:195], v161
	v_add_u32_e32 v160, v2, v110
	s_waitcnt lgkmcnt(2)
	v_mfma_f32_16x16x32_bf16 v[180:183], v[188:191], v[196:199], v[180:183]
	v_cvt_pk_bf16_f32 v188, v18, v19
	v_cvt_pk_bf16_f32 v189, v20, v21
	v_cvt_pk_bf16_f32 v190, v10, v11
	v_cvt_pk_bf16_f32 v191, v12, v13
	v_add_u32_e32 v161, v2, v111
	ds_read_b64 v[196:197], v160
	ds_read_b64 v[198:199], v161
	v_lshlrev_b32_e32 v3, 16, v159
	v_cvt_pk_bf16_f32 v160, v3, v5
	v_add_u32_e32 v3, v0, v112
	v_lshlrev_b32_e32 v51, 16, v165
	v_lshlrev_b32_e32 v55, 16, v163
	v_lshlrev_b32_e32 v159, 16, v166
	s_waitcnt lgkmcnt(2)
	v_mfma_f32_16x16x32_bf16 v[184:187], v[188:191], v[192:195], v[184:187]
	v_lshlrev_b32_e32 v166, 16, v162
	v_lshlrev_b32_e32 v171, 16, v164
	v_add_u32_e32 v0, v0, v113
	s_waitcnt lgkmcnt(0)
	v_mfma_f32_16x16x32_bf16 v[180:183], v[188:191], v[196:199], v[180:183]
	v_cvt_pk_bf16_f32 v188, v6, v7
	v_cvt_pk_bf16_f32 v189, v8, v9
	v_cvt_pk_bf16_f32 v190, v14, v15
	v_cvt_pk_bf16_f32 v191, v16, v17
	ds_read_b64 v[162:163], v3
	ds_read_b64 v[164:165], v0
	v_add_u32_e32 v0, v2, v112
	v_add_u32_e32 v2, v2, v113
	ds_read_b64 v[192:193], v0
	ds_read_b64 v[194:195], v2
	s_waitcnt lgkmcnt(2)
	v_mfma_f32_16x16x32_bf16 v[184:187], v[188:191], v[162:165], v[184:187]
	v_add_u32_e32 v0, s54, v64
	v_add_u32_e32 v3, s55, v1
	v_cndmask_b32_e64 v2, v0, v3, s[18:19]
	v_add_u32_e32 v0, s54, v65
	v_add_u32_e32 v3, 16, v3
	s_waitcnt lgkmcnt(0)
	v_mfma_f32_16x16x32_bf16 v[180:183], v[188:191], v[192:195], v[180:183]
	v_cndmask_b32_e64 v164, v0, v3, s[18:19]
	v_ashrrev_i32_e32 v3, 31, v2
	v_lshlrev_b64 v[2:3], 11, v[2:3]
	v_cvt_pk_bf16_f32 v176, v184, v185
	v_cvt_pk_bf16_f32 v177, v186, v187
	v_lshl_add_u64 v[2:3], v[42:43], 0, v[2:3]
	v_add_u32_e32 v0, s57, v61
	v_cvt_pk_bf16_f32 v161, v51, v53
	global_store_dwordx2 v[2:3], v[176:177], off
	v_lshl_add_u32 v5, v40, 2, s57
	v_add_u32_e32 v53, v0, v114
	v_cvt_pk_bf16_f32 v204, v180, v181
	v_cvt_pk_bf16_f32 v205, v182, v183
	v_add_u32_e32 v51, v0, v96
	ds_read_b128 v[180:183], v5 offset:24576
	ds_read_b128 v[184:187], v51 offset:16384
	ds_read_b128 v[192:195], v53 offset:16384
	ds_read_b128 v[188:191], v5 offset:24640
	v_cvt_pk_bf16_f32 v162, v55, v159
	v_cvt_pk_bf16_f32 v163, v166, v171
	s_waitcnt lgkmcnt(3)
	v_mul_f32_e32 v36, v36, v182
	v_mul_f32_e32 v37, v37, v183
	v_mul_f32_e32 v34, v34, v180
	v_mul_f32_e32 v35, v35, v181
	ds_read_b128 v[180:183], v51 offset:20480
	s_waitcnt lgkmcnt(1)
	v_mul_f32_e32 v32, v32, v190
	v_mul_f32_e32 v33, v33, v191
	v_mul_f32_e32 v30, v30, v188
	v_mul_f32_e32 v31, v31, v189
	v_add_u32_e32 v53, v0, v115
	v_mfma_f32_16x16x32_bf16 v[34:37], v[184:187], v[160:163], v[34:37]
	ds_read_b128 v[184:187], v53 offset:16384
	ds_read_b128 v[188:191], v51 offset:23552
	v_add_u32_e32 v0, v0, v116
	v_ashrrev_i32_e32 v165, 31, v164
	v_mfma_f32_16x16x32_bf16 v[30:33], v[192:195], v[160:163], v[30:33]
	ds_read_b128 v[192:195], v5 offset:24704
	ds_read_b128 v[196:199], v0 offset:16384
	ds_read_b128 v[200:203], v5 offset:24768
	v_lshlrev_b64 v[2:3], 11, v[164:165]
	s_add_i32 s55, s55, 32
	s_sub_i32 s54, s54, 32
	s_waitcnt lgkmcnt(2)
	v_mul_f32_e32 v28, v28, v194
	v_mul_f32_e32 v29, v29, v195
	v_mul_f32_e32 v26, v26, v192
	v_mul_f32_e32 v27, v27, v193
	s_waitcnt lgkmcnt(0)
	v_mul_f32_e32 v24, v24, v202
	v_mul_f32_e32 v25, v25, v203
	v_mul_f32_e32 v22, v22, v200
	v_mul_f32_e32 v23, v23, v201
	v_mfma_f32_16x16x32_bf16 v[26:29], v[184:187], v[160:163], v[26:29]
	ds_read_b128 v[184:187], v5 offset:24832
	v_lshl_add_u64 v[2:3], v[42:43], 0, v[2:3]
	s_cmpk_eq_i32 s55, 0x7e0
	v_mfma_f32_16x16x32_bf16 v[22:25], v[196:199], v[160:163], v[22:25]
	ds_read_b128 v[192:195], v51 offset:21504
	ds_read_b128 v[196:199], v5 offset:24896
	s_waitcnt lgkmcnt(2)
	v_mul_f32_e32 v20, v20, v186
	v_mul_f32_e32 v21, v21, v187
	v_mul_f32_e32 v18, v18, v184
	v_mul_f32_e32 v19, v19, v185
	ds_read_b128 v[184:187], v5 offset:24960
	global_store_dwordx2 v[2:3], v[204:205], off
	v_mfma_f32_16x16x32_bf16 v[18:21], v[180:183], v[160:163], v[18:21]
	ds_read_b128 v[180:183], v51 offset:22528
	s_waitcnt lgkmcnt(2)
	v_mul_f32_e32 v12, v12, v198
	v_mul_f32_e32 v13, v13, v199
	v_mul_f32_e32 v10, v10, v196
	v_mul_f32_e32 v11, v11, v197
	s_nop 1
	v_mfma_f32_16x16x32_bf16 v[10:13], v[192:195], v[160:163], v[10:13]
	ds_read_b128 v[192:195], v5 offset:25024
	s_waitcnt lgkmcnt(2)
	v_mul_f32_e32 v8, v8, v186
	v_mul_f32_e32 v9, v9, v187
	v_mul_f32_e32 v6, v6, v184
	v_mul_f32_e32 v7, v7, v185
	s_waitcnt lgkmcnt(0)
	v_mul_f32_e32 v16, v16, v194
	v_mul_f32_e32 v17, v17, v195
	v_mul_f32_e32 v14, v14, v192
	v_mul_f32_e32 v15, v15, v193
	v_mfma_f32_16x16x32_bf16 v[6:9], v[180:183], v[160:163], v[6:9]
	s_nop 0
	v_mfma_f32_16x16x32_bf16 v[14:17], v[188:191], v[160:163], v[14:17]
	s_cbranch_scc1 .LBB0_279
	s_waitcnt vmcnt(4)
	v_mov_b32_e32 v164, v179
	v_mov_b32_e32 v162, v178
	v_mov_b32_e32 v166, v174
	v_mov_b32_e32 v163, v173
	v_mov_b32_e32 v161, v170
	v_mov_b32_e32 v165, v169
	v_mov_b32_e32 v160, v168
	v_mov_b32_e32 v159, v167
	s_waitcnt vmcnt(2)
	v_mov_b32_e32 v181, v152
	v_mov_b32_e32 v180, v150
	v_mov_b32_e32 v176, v148
	v_mov_b32_e32 v177, v147
	v_mov_b32_e32 v172, v142
	v_mov_b32_e32 v175, v146
	v_mov_b32_e32 v5, v140
	v_mov_b32_e32 v171, v143
	s_branch .LBB0_275
; #define LAS __attribute__((address_space(3)))
; __device__ __forceinline__ float bf2f(bf16_t v) { return __uint_as_float((unsigned)v << 16); }
; __device__ __forceinline__ bf16_t f2bf(float a) { return (bf16_t)(pk2(a, 0.f) & 0xffffu); }
; __device__ __forceinline__ float frcp(float x) { return __builtin_amdgcn_rcpf(x); }
; __device__ __forceinline__ float sigm(float x) { return frcp(1.f + __expf(-x)); }
; __device__ __forceinline__ float silu(float x) { return x * frcp(1.f + __expf(-x)); }
; __device__ __forceinline__ void hgrn_mfma(const Params& p, LAS unsigned char* lds) {
;     ...
;             float qv[8], fv[8], vv[8], vp[8];
; #pragma unroll
;             for (int i = 0; i < 8; ++i) { qv[i] = bf2f(rq[i]); vv[i] = bf2f(rv[i]); fv[i] = bf2f(rz[i]); vp[i] = bf2f(rp[i]); }
;             if (n + 1 < T / 32) HG_LOAD(n + 1);
;             float Pl[8]; float P = 1.f;
; #pragma unroll
;             for (int i = 0; i < 8; ++i) { fv[i] = lb + (1.f - lb) * sigm(fv[i]); P *= fv[i]; Pl[i] = P; }
;             const float p0 = __shfl(P, fr), p1 = __shfl(P, fr + 16), p2 = __shfl(P, fr + 32), p3 = __shfl(P, fr + 48);
;             const float pre = (fq > 0 ? p0 : 1.f) * (fq > 1 ? p1 : 1.f) * (fq > 2 ? p2 : 1.f), tot = (p0 * p1) * (p2 * p3);
;             float kd[8];
; #pragma unroll
;             for (int i = 0; i < 8; ++i) {
;                 const int c = 8 * fq + i; const float E = pre * Pl[i], rE = frcp(E), k = 1.f - fv[i];
;                 *(LAS bf16_t*)(QG + rm_byte(c, d)) = f2bf(silu(qv[i]) * E);
;                 *(LAS bf16_t*)(KG + rm_byte(c, d)) = f2bf(k * rE);
;                 kd[i] = k * tot * rE;
;             }
.LBB0_279:
	s_waitcnt vmcnt(11)
	v_lshlrev_b32_e32 v53, 16, v154
	v_mul_f32_e32 v53, 0xbfb8aa3b, v53
	v_exp_f32_e32 v53, v53
	v_lshlrev_b32_e32 v151, 16, v151
	v_lshlrev_b32_e32 v2, 16, v138
	v_lshlrev_b32_e32 v138, 16, v136
	v_mul_f32_e32 v136, 0xbfb8aa3b, v151
	v_exp_f32_e32 v136, v136
	v_add_f32_e32 v53, 1.0, v53
	v_lshlrev_b32_e32 v3, 16, v137
	v_rcp_f32_e32 v137, v53
	s_waitcnt vmcnt(7)
	v_lshlrev_b32_e32 v51, 16, v156
	v_mul_f32_e32 v51, 0xbfb8aa3b, v51
	v_lshlrev_b32_e32 v55, 16, v141
	v_lshlrev_b32_e32 v141, 16, v139
	v_lshlrev_b32_e32 v135, 16, v135
	v_exp_f32_e32 v139, v51
	v_add_f32_e32 v51, 1.0, v136
	v_mul_f32_e32 v3, 0xbfb8aa3b, v3
	v_mul_f32_e32 v2, 0xbfb8aa3b, v2
	v_rcp_f32_e32 v53, v51
	v_fma_f32 v51, v52, v137, v50
	v_mul_f32_e32 v137, 0xbfb8aa3b, v135
	v_exp_f32_e32 v3, v3
	v_exp_f32_e32 v44, v2
	v_exp_f32_e32 v137, v137
	s_waitcnt vmcnt(3)
	v_lshlrev_b32_e32 v0, 16, v158
	v_mul_f32_e32 v0, 0xbfb8aa3b, v0
	v_add_f32_e32 v2, 1.0, v3
	v_add_f32_e32 v3, 1.0, v44
	v_exp_f32_e32 v0, v0
	v_add_f32_e32 v137, 1.0, v137
	v_rcp_f32_e32 v2, v2
	v_rcp_f32_e32 v3, v3
	v_add_f32_e32 v136, 1.0, v139
	v_rcp_f32_e32 v139, v137
	v_mul_f32_e32 v137, 0xbfb8aa3b, v138
	v_lshlrev_b32_e32 v54, 16, v145
	v_exp_f32_e32 v145, v137
	v_add_f32_e32 v0, 1.0, v0
	v_lshlrev_b32_e32 v144, 16, v144
	v_fma_f32 v44, v48, v2, v46
	v_fma_f32 v45, v49, v3, v47
	v_mul_f32_e32 v2, 0xbfb8aa3b, v55
	v_mul_f32_e32 v3, 0xbfb8aa3b, v54
	v_rcp_f32_e32 v137, v0
	v_mul_f32_e32 v0, v139, v135
	v_mul_f32_e32 v139, 0xbfb8aa3b, v141
	v_exp_f32_e32 v2, v2
	v_exp_f32_e32 v3, v3
	v_add_f32_e32 v135, 1.0, v145
	v_exp_f32_e32 v139, v139
	v_mul_f32_e32 v145, 0xbfb8aa3b, v144
	v_exp_f32_e32 v145, v145
	v_add_f32_e32 v2, 1.0, v2
	v_add_f32_e32 v3, 1.0, v3
	v_add_f32_e32 v139, 1.0, v139
	v_rcp_f32_e32 v2, v2
	v_rcp_f32_e32 v3, v3
	v_rcp_f32_e32 v151, v139
	v_add_f32_e32 v139, 1.0, v145
	v_rcp_f32_e32 v145, v139
	v_pk_mul_f32 v[54:55], v[44:45], v[44:45] op_sel:[0,1] op_sel_hi:[1,0]
	v_fma_f32 v2, v48, v2, v46
	v_fma_f32 v3, v49, v3, v47
	v_lshlrev_b32_e32 v5, 16, v157
	v_lshlrev_b32_e32 v158, 16, v155
	v_mul_f32_e32 v141, v151, v141
	v_mul_f32_e32 v151, v145, v144
	v_mov_b32_e32 v144, v54
	v_mov_b32_e32 v145, v52
	v_mov_b32_e32 v52, v2
	v_mov_b32_e32 v156, v3
	v_mov_b32_e32 v157, v50
	v_fma_f32 v52, v144, v52, v156
	v_fma_f32 v53, v145, v53, v157
	v_mul_f32_e32 v144, 0xbfb8aa3b, v158
	v_exp_f32_e32 v156, v144
	v_mul_f32_e32 v154, v54, v2
	v_mul_f32_e32 v155, v55, v3
	v_rcp_f32_e32 v135, v135
	v_mul_f32_e32 v52, v154, v3
	v_pk_add_f32 v[144:145], v[2:3], 1.0 op_sel_hi:[1,0] neg_lo:[1,0] neg_hi:[1,0]
	v_add_f32_e32 v2, 1.0, v156
	v_mul_f32_e32 v3, 0xbfb8aa3b, v5
	v_rcp_f32_e32 v2, v2
	v_exp_f32_e32 v3, v3
	v_rcp_f32_e32 v136, v136
	v_lshlrev_b32_e32 v153, 16, v153
	v_lshlrev_b32_e32 v149, 16, v149
	v_mul_f32_e32 v135, v135, v138
	v_pk_add_f32 v[138:139], v[44:45], 1.0 op_sel_hi:[1,0] neg_lo:[1,0] neg_hi:[1,0]
	v_mul_f32_e32 v45, 0xbfb8aa3b, v149
	v_mul_f32_e32 v50, 0xbfb8aa3b, v153
	v_mul_f32_e32 v55, v52, v53
	v_exp_f32_e32 v45, v45
	v_exp_f32_e32 v50, v50
	v_mul_f32_e32 v156, v2, v158
	v_add_f32_e32 v2, 1.0, v3
	v_mul_f32_e32 v155, v55, v51
	v_rcp_f32_e32 v3, v2
	v_fma_f32 v46, v48, v136, v46
	v_fma_f32 v47, v49, v137, v47
	v_add_f32_e32 v45, 1.0, v45
	v_mul_f32_e32 v136, v155, v46
	v_mul_f32_e32 v137, v136, v47
	v_add_f32_e32 v50, 1.0, v50
	ds_bpermute_b32 v2, v56, v137
	ds_bpermute_b32 v48, v57, v137
	v_rcp_f32_e32 v45, v45
	v_rcp_f32_e32 v50, v50
	v_mul_f32_e32 v5, v3, v5
	ds_bpermute_b32 v3, v58, v137
	v_mul_f32_e32 v149, v45, v149
	v_mul_f32_e32 v153, v50, v153
	v_mov_b32_e32 v50, v53
	ds_bpermute_b32 v49, v59, v137
	s_waitcnt lgkmcnt(3)
; #define LAS __attribute__((address_space(3)))
; __device__ __forceinline__ unsigned pk2(float a, float b) { f32x2 v = {a, b}; bf16x2_t r = __builtin_convertvector(v, bf16x2_t); return __builtin_bit_cast(unsigned, r); }
; __device__ __forceinline__ bf16_t f2bf(float a) { return (bf16_t)(pk2(a, 0.f) & 0xffffu); }
; __device__ __forceinline__ float frcp(float x) { return __builtin_amdgcn_rcpf(x); }
; __device__ __forceinline__ float silu(float x) { return x * frcp(1.f + __expf(-x)); }
; __device__ __forceinline__ void hgrn_mfma(const Params& p, LAS unsigned char* lds) {
;     ...
;             const float p0 = __shfl(P, fr), p1 = __shfl(P, fr + 16), p2 = __shfl(P, fr + 32), p3 = __shfl(P, fr + 48);
;             const float pre = (fq > 0 ? p0 : 1.f) * (fq > 1 ? p1 : 1.f) * (fq > 2 ? p2 : 1.f), tot = (p0 * p1) * (p2 * p3);
;             float kd[8];
; #pragma unroll
;             for (int i = 0; i < 8; ++i) {
;                 const int c = 8 * fq + i; const float E = pre * Pl[i], rE = frcp(E), k = 1.f - fv[i];
;                 *(LAS bf16_t*)(QG + rm_byte(c, d)) = f2bf(silu(qv[i]) * E);
;                 *(LAS bf16_t*)(KG + rm_byte(c, d)) = f2bf(k * rE);
;                 kd[i] = k * tot * rE;
;             }
;             { u32x4 wv; wv.x = pk2(kd[0], kd[1]); wv.y = pk2(kd[2], kd[3]); wv.z = pk2(kd[4], kd[5]); wv.w = pk2(kd[6], kd[7]);
;               *(LAS u32x4*)(KDT + d * 64 + ((fq ^ ((d >> 2) & 3)) << 4)) = wv; }
;             if (fq == 0) DEC[d] = tot;
	v_cndmask_b32_e64 v45, v2, 1.0, s[4:5]
	s_waitcnt lgkmcnt(2)
	v_cndmask_b32_e64 v53, 1.0, v48, s[6:7]
	v_mul_f32_e32 v45, v45, v53
	s_waitcnt lgkmcnt(1)
	v_cndmask_b32_e64 v53, 1.0, v3, s[8:9]
	v_mul_f32_e32 v157, v45, v53
	v_mul_f32_e32 v45, v44, v157
	v_rcp_f32_e32 v44, v45
	v_mul_f32_e32 v0, v0, v45
	s_waitcnt lgkmcnt(0)
	v_mul_f32_e32 v2, v2, v48
	v_mul_f32_e32 v3, v3, v49
	v_cvt_pk_bf16_f32 v0, v0, s0
	v_add_u32_e32 v48, 0, v97
	ds_write_b16 v48, v0 offset:25088
	v_mul_f32_e32 v0, v54, v157
	v_rcp_f32_e32 v45, v0
	v_mul_f32_e32 v49, v138, v44
	v_pk_mul_f32 v[2:3], v[2:3], v[2:3] op_sel:[0,1] op_sel_hi:[1,0]
	v_cvt_pk_bf16_f32 v49, v49, s0
	v_mul_f32_e32 v0, v135, v0
	ds_write_b16 v48, v49 offset:33280
	v_pk_mul_f32 v[48:49], v[138:139], v[2:3] op_sel_hi:[1,0]
	v_cvt_pk_bf16_f32 v0, v0, s0
	v_mul_f32_e32 v48, v44, v48
	v_mul_f32_e32 v49, v45, v49
	v_add_u32_e32 v44, 0, v125
	ds_write_b16 v44, v0 offset:25344
	v_mul_f32_e32 v0, v139, v45
	v_cvt_pk_bf16_f32 v0, v0, s0
	ds_write_b16 v44, v0 offset:33536
	v_mul_f32_e32 v0, v154, v157
	v_rcp_f32_e32 v44, v0
	v_mul_f32_e32 v0, v141, v0
	v_mul_f32_e32 v54, v52, v157
	v_cvt_pk_bf16_f32 v0, v0, s0
	v_add_u32_e32 v53, 0, v126
	v_rcp_f32_e32 v45, v54
	ds_write_b16 v53, v0 offset:25600
	v_mul_f32_e32 v0, v144, v44
	v_cvt_pk_bf16_f32 v0, v0, s0
	ds_write_b16 v53, v0 offset:33792
	v_pk_mul_f32 v[52:53], v[144:145], v[2:3] op_sel_hi:[1,0]
	v_mul_f32_e32 v0, v151, v54
	v_mul_f32_e32 v52, v44, v52
	v_mul_f32_e32 v53, v45, v53
	v_cvt_pk_bf16_f32 v0, v0, s0
	v_add_u32_e32 v44, 0, v127
	ds_write_b16 v44, v0 offset:25856
	v_mul_f32_e32 v0, v145, v45
	v_cvt_pk_bf16_f32 v0, v0, s0
	ds_write_b16 v44, v0 offset:34048
	v_mul_f32_e32 v0, v55, v157
	v_rcp_f32_e32 v44, v0
	v_mul_f32_e32 v0, v149, v0
	v_cvt_pk_bf16_f32 v0, v0, s0
	v_add_u32_e32 v54, 0, v128
	ds_write_b16 v54, v0 offset:26112
	v_mul_f32_e32 v0, v155, v157
	v_pk_add_f32 v[50:51], v[50:51], 1.0 op_sel_hi:[1,0] neg_lo:[1,0] neg_hi:[1,0]
	v_rcp_f32_e32 v45, v0
	v_mul_f32_e32 v55, v50, v44
	v_cvt_pk_bf16_f32 v55, v55, s0
	v_mul_f32_e32 v0, v153, v0
	ds_write_b16 v54, v55 offset:34304
	v_pk_mul_f32 v[54:55], v[50:51], v[2:3] op_sel_hi:[1,0]
	v_cvt_pk_bf16_f32 v0, v0, s0
	v_mul_f32_e32 v54, v44, v54
	v_mul_f32_e32 v55, v45, v55
	v_add_u32_e32 v44, 0, v129
	ds_write_b16 v44, v0 offset:26368
	v_mul_f32_e32 v0, v51, v45
	v_cvt_pk_bf16_f32 v0, v0, s0
	ds_write_b16 v44, v0 offset:34560
	v_mul_f32_e32 v0, v136, v157
	v_rcp_f32_e32 v44, v0
	v_mul_f32_e32 v0, v156, v0
	v_cvt_pk_bf16_f32 v0, v0, s0
	v_add_u32_e32 v50, 0, v130
	v_pk_add_f32 v[46:47], v[46:47], 1.0 op_sel_hi:[1,0] neg_lo:[1,0] neg_hi:[1,0]
	v_mul_f32_e32 v135, v137, v157
	ds_write_b16 v50, v0 offset:26624
	v_mul_f32_e32 v0, v46, v44
	v_rcp_f32_e32 v45, v135
	v_cvt_pk_bf16_f32 v0, v0, s0
	ds_write_b16 v50, v0 offset:34816
	v_mul_f32_e32 v0, v5, v135
	v_pk_mul_f32 v[50:51], v[46:47], v[2:3] op_sel_hi:[1,0]
	v_cvt_pk_bf16_f32 v0, v0, s0
	v_add_u32_e32 v3, 0, v131
	ds_write_b16 v3, v0 offset:26880
	v_mul_f32_e32 v0, v47, v45
	v_mul_f32_e32 v50, v44, v50
	v_mul_f32_e32 v51, v45, v51
	v_cvt_pk_bf16_f32 v0, v0, s0
	ds_write_b16 v3, v0 offset:35072
	v_cvt_pk_bf16_f32 v44, v48, v49
	v_cvt_pk_bf16_f32 v45, v52, v53
	v_cvt_pk_bf16_f32 v46, v54, v55
	v_cvt_pk_bf16_f32 v47, v50, v51
	v_add_u32_e32 v0, v117, v61
	ds_write_b128 v0, v[44:47] offset:41472
	s_and_saveexec_b64 s[46:47], s[4:5]
	s_cbranch_execz .LBB0_273
	v_add_u32_e32 v0, v117, v118
	ds_write_b32 v0, v2 offset:49664
	s_branch .LBB0_273

; __device__ __forceinline__ int crow(int r, int hi) { return (r & 3) + 8 * (r >> 2) + 4 * hi; }
; __device__ __forceinline__ void partialSM(f32x16& p0, f32x16& p1, float& m_reg, float& mn, float& alpha) {
;     ...
;   else { mn = fmaxf(m_reg, pmax); alpha = __builtin_amdgcn_exp2f((m_reg - mn) * C); m_reg = mn; }
; template <int LDQ, int LDK, int LDO>
; __device__ __forceinline__ void attn_body256(const bf16_t* __restrict__ Qb, const bf16_t* __restrict__ Kh, const bf16_t* __restrict__ Vh, float* __restrict__ Ob, int seq, LAS char* lds) {
;     ...
;     if (__any(al < 1.f)) { if (hi == 0) al_l[r32] = al; asm volatile("s_waitcnt lgkmcnt(0)" ::: "memory");
; #pragma unroll
;       for (int d = 0; d < 8; ++d)
; #pragma unroll
;         for (int r = 0; r < 16; ++r) o[d][r] *= al_l[crow(r, hi)]; }
.LBB0_938:
	v_sub_f32_e32 v0, v248, v249
	v_mul_f32_e32 v0, 0x3e0293ee, v0
	v_exp_f32_e32 v0, v0
	s_nop 0
	v_cndmask_b32_e64 v220, v0, 1.0, s[10:11]
	v_cmp_gt_f32_e32 vcc, 1.0, v220
	s_cbranch_vccz .LBB0_942
	s_and_saveexec_b64 s[10:11], s[6:7]
	ds_write_b32 v243, v220 offset:128
	s_or_b64 exec, exec, s[10:11]
	s_waitcnt lgkmcnt(0)
	v_add_u32_e32 v0, v232, v212
	ds_read_b128 v[160:163], v0 offset:224
	ds_read_b128 v[156:159], v0 offset:192
	ds_read_b128 v[152:155], v0 offset:160
	ds_read_b128 v[148:151], v0 offset:128
	s_waitcnt lgkmcnt(3)
	v_mul_f32_e32 v128, v128, v160
	v_mul_f32_e32 v129, v129, v161
	s_waitcnt lgkmcnt(2)
	v_mul_f32_e32 v124, v124, v156
	v_mul_f32_e32 v125, v125, v157
	s_waitcnt lgkmcnt(1)
	v_mul_f32_e32 v120, v120, v152
	v_mul_f32_e32 v121, v121, v153
	v_mul_f32_e32 v130, v130, v162
	v_mul_f32_e32 v131, v131, v163
	v_mul_f32_e32 v126, v126, v158
	v_mul_f32_e32 v127, v127, v159
	v_mul_f32_e32 v122, v122, v154
	v_mul_f32_e32 v123, v123, v155
	s_waitcnt lgkmcnt(0)
	v_mul_f32_e32 v118, v118, v150
	v_mul_f32_e32 v119, v119, v151
	v_mul_f32_e32 v116, v116, v148
	v_mul_f32_e32 v117, v117, v149
	v_mul_f32_e32 v112, v112, v160
	v_mul_f32_e32 v113, v113, v161
	v_mul_f32_e32 v108, v108, v156
	v_mul_f32_e32 v109, v109, v157
	v_mul_f32_e32 v104, v104, v152
	v_mul_f32_e32 v105, v105, v153
	v_mul_f32_e32 v114, v114, v162
	v_mul_f32_e32 v115, v115, v163
	v_mul_f32_e32 v110, v110, v158
	v_mul_f32_e32 v111, v111, v159
	v_mul_f32_e32 v106, v106, v154
	v_mul_f32_e32 v107, v107, v155
	v_mul_f32_e32 v102, v102, v150
	v_mul_f32_e32 v103, v103, v151
	v_mul_f32_e32 v100, v100, v148
	v_mul_f32_e32 v101, v101, v149
	v_mul_f32_e32 v96, v96, v160
	v_mul_f32_e32 v97, v97, v161
	v_mul_f32_e32 v92, v92, v156
	v_mul_f32_e32 v93, v93, v157
	v_mul_f32_e32 v88, v88, v152
	v_mul_f32_e32 v89, v89, v153
	v_mul_f32_e32 v98, v98, v162
	v_mul_f32_e32 v99, v99, v163
	v_mul_f32_e32 v94, v94, v158
	v_mul_f32_e32 v95, v95, v159
	v_mul_f32_e32 v90, v90, v154
	v_mul_f32_e32 v91, v91, v155
	v_mul_f32_e32 v86, v86, v150
	v_mul_f32_e32 v87, v87, v151
	v_mul_f32_e32 v84, v84, v148
	v_mul_f32_e32 v85, v85, v149
	v_mul_f32_e32 v80, v80, v160
	v_mul_f32_e32 v81, v81, v161
	v_mul_f32_e32 v76, v76, v156
	v_mul_f32_e32 v77, v77, v157
	v_mul_f32_e32 v72, v72, v152
	v_mul_f32_e32 v73, v73, v153
	v_mul_f32_e32 v82, v82, v162
	v_mul_f32_e32 v83, v83, v163
	v_mul_f32_e32 v78, v78, v158
	v_mul_f32_e32 v79, v79, v159
	v_mul_f32_e32 v74, v74, v154
	v_mul_f32_e32 v75, v75, v155
	v_mul_f32_e32 v70, v70, v150
	v_mul_f32_e32 v71, v71, v151
	v_mul_f32_e32 v68, v68, v148
	v_mul_f32_e32 v69, v69, v149
	v_mul_f32_e32 v64, v64, v160
	v_mul_f32_e32 v65, v65, v161
	v_mul_f32_e32 v60, v60, v156
	v_mul_f32_e32 v61, v61, v157
	v_mul_f32_e32 v56, v56, v152
	v_mul_f32_e32 v57, v57, v153
	v_mul_f32_e32 v66, v66, v162
	v_mul_f32_e32 v67, v67, v163
	v_mul_f32_e32 v62, v62, v158
	v_mul_f32_e32 v63, v63, v159
	v_mul_f32_e32 v58, v58, v154
	v_mul_f32_e32 v59, v59, v155
	v_mul_f32_e32 v54, v54, v150
	v_mul_f32_e32 v55, v55, v151
	v_mul_f32_e32 v52, v52, v148
	v_mul_f32_e32 v53, v53, v149
	v_mul_f32_e32 v48, v48, v160
	v_mul_f32_e32 v49, v49, v161
	v_mul_f32_e32 v44, v44, v156
	v_mul_f32_e32 v45, v45, v157
	v_mul_f32_e32 v40, v40, v152
	v_mul_f32_e32 v41, v41, v153
	v_mul_f32_e32 v50, v50, v162
	v_mul_f32_e32 v51, v51, v163
	v_mul_f32_e32 v46, v46, v158
	v_mul_f32_e32 v47, v47, v159
	v_mul_f32_e32 v42, v42, v154
	v_mul_f32_e32 v43, v43, v155
	v_mul_f32_e32 v38, v38, v150
	v_mul_f32_e32 v39, v39, v151
	v_mul_f32_e32 v36, v36, v148
	v_mul_f32_e32 v37, v37, v149
	v_mul_f32_e32 v32, v32, v160
	v_mul_f32_e32 v33, v33, v161
	v_mul_f32_e32 v28, v28, v156
	v_mul_f32_e32 v29, v29, v157
	v_mul_f32_e32 v24, v24, v152
	v_mul_f32_e32 v25, v25, v153
	v_mul_f32_e32 v34, v34, v162
	v_mul_f32_e32 v35, v35, v163
	v_mul_f32_e32 v30, v30, v158
	v_mul_f32_e32 v31, v31, v159
	v_mul_f32_e32 v26, v26, v154
	v_mul_f32_e32 v27, v27, v155
	v_mul_f32_e32 v22, v22, v150
	v_mul_f32_e32 v23, v23, v151
	v_mul_f32_e32 v20, v20, v148
	v_mul_f32_e32 v21, v21, v149
	v_mul_f32_e32 v16, v16, v160
	v_mul_f32_e32 v17, v17, v161
	v_mul_f32_e32 v12, v12, v156
	v_mul_f32_e32 v13, v13, v157
	v_mul_f32_e32 v8, v8, v152
	v_mul_f32_e32 v9, v9, v153
	v_mul_f32_e32 v18, v18, v162
	v_mul_f32_e32 v19, v19, v163
	v_mul_f32_e32 v14, v14, v158
	v_mul_f32_e32 v15, v15, v159
	v_mul_f32_e32 v10, v10, v154
	v_mul_f32_e32 v11, v11, v155
	v_mul_f32_e32 v6, v6, v150
	v_mul_f32_e32 v7, v7, v151
	v_mul_f32_e32 v4, v4, v148
	v_mul_f32_e32 v5, v5, v149
